# P5 QK: first 8 MFMAs wait only for key-group-0 fragments (lgkmcnt 8 then 0), on top of v29
# speedup vs baseline: 1.0148x; 1.0050x over previous
; #define LAS __attribute__((address_space(3)))
; #define TA_SB __builtin_amdgcn_sched_barrier(0)
; __device__ __forceinline__ void ta_ldk(LAS const unsigned char* kb, int kg, int i, int g4, bf16x8 (&a0)[4], bf16x8 (&a1)[4]) {
;     LAS const unsigned char* kr = kb + (32 * kg + 8 * (i >> 2) + (i & 3)) * 256;
; #pragma unroll
;     for (int ks = 0; ks < 4; ++ks) { const int co = ((4 * ks + g4) ^ i) * 16; a0[ks] = *(LAS const bf16x8*)(kr + co); a1[ks] = *(LAS const bf16x8*)(kr + 4 * 256 + co); } }
; __device__ __forceinline__ void ta_ldv(LAS const unsigned char* vb, int kg, int i, int g4, bf16x8 (&vt)[8]) {
;     LAS const unsigned char* vr = vb + i * 128 + (((4 * kg + g4) ^ ((i >> 1) & 7)) * 16);
; #pragma unroll
;     for (int dt = 0; dt < 8; ++dt) vt[dt] = *(LAS const bf16x8*)(vr + dt * 16 * 128); }
; __device__ __forceinline__ void ta_qk(const bf16x8 (&a0)[4], const bf16x8 (&a1)[4], const QF& q, f32x4& s0, f32x4& s1) {
;     s0 = (f32x4){0.f, 0.f, 0.f, 0.f}; s1 = (f32x4){0.f, 0.f, 0.f, 0.f};
; #pragma unroll
;     for (int ks = 0; ks < 4; ++ks) { s0 = __builtin_amdgcn_mfma_f32_16x16x32_bf16(a0[ks], q.f[ks], s0, 0, 0, 0); s1 = __builtin_amdgcn_mfma_f32_16x16x32_bf16(a1[ks], q.f[ks], s1, 0, 0, 0); } }
; template <int MODE, bool FULL = false> __device__ __forceinline__ void ta_compute2(LAS const unsigned char* kb, const QF& q0, const QF& q1, f32x4 (&O0)[8], f32x4 (&O1)[8], float& l0, float& l1, int i, int g4, int tq0, int tq1, bool n0, bool n1, bool cv0, bool cv1, int kbase, float mb, bool full = fa ...
;     LAS const unsigned char* vb = kb + 16384;
;     const float m0 = cv0 ? mb : 1e30f, m1 = cv1 ? mb : 1e30f;
;     bf16x8 ka0[4], ka1[4], kb0[4], kb1[4], va[8], vc[8]; f32x4 s0, s1, t0, t1, u0, u1, v0, v1; bf16x8 pa0, pb0, pa1, pb1;
;     ta_ldk(kb, 0, i, g4, ka0, ka1); ta_ldk(kb, 1, i, g4, kb0, kb1); TA_SB;
;     if (n0) { ta_qk(ka0, ka1, q0, s0, s1); ta_qk(kb0, kb1, q0, t0, t1); } TA_SB;
;     if (n1) { ta_qk(ka0, ka1, q1, u0, u1); ta_qk(kb0, kb1, q1, v0, v1); } TA_SB;
.LBB0_699:
	s_and_b32 s90, s84, 0xff
	s_lshl_b32 s90, s90, 5
	s_add_i32 s90, s90, s59
	s_and_b32 s91, s85, 0xff
	s_lshl_b32 s91, s91, 5
	s_add_i32 s91, s91, s59
	v_mov_b32_e32 v250, s90
	v_mov_b32_e32 v251, s91
	v_mov_b32_e32 v249, s22
	ds_read_b32 v250, v250
	ds_read_b32 v251, v251
	ds_read_b64 v[252:253], v249 offset:16
	v_mov_b32_e32 v215, s86
	s_and_b32 s0, s75, 0x10000
	s_mov_b32 s78, s88
	s_cmp_eq_u32 s78, 0
	s_cbranch_scc1 .LBB0_723
	s_add_i32 s14, s0, 0
	v_add_u32_e32 v122, s14, v233
	v_add_u32_e32 v130, v122, v234
	v_add_u32_e32 v131, v122, v235
	v_add_u32_e32 v132, v122, v236
	v_add_u32_e32 v133, v122, v237
	ds_read_b128 v[98:101], v130
	ds_read_b128 v[102:105], v130 offset:1024
	ds_read_b128 v[106:109], v131
	ds_read_b128 v[110:113], v131 offset:1024
	ds_read_b128 v[114:117], v132
	ds_read_b128 v[118:121], v132 offset:1024
	ds_read_b128 v[122:125], v133
	ds_read_b128 v[126:129], v133 offset:1024
	ds_read_b128 v[146:149], v130 offset:8192
	ds_read_b128 v[150:153], v130 offset:9216
	ds_read_b128 v[170:173], v131 offset:8192
	ds_read_b128 v[174:177], v131 offset:9216
	ds_read_b128 v[178:181], v132 offset:8192
	ds_read_b128 v[182:185], v132 offset:9216
	ds_read_b128 v[186:189], v133 offset:8192
	ds_read_b128 v[190:193], v133 offset:9216
	s_and_b32 s15, s78, 15
	s_cmp_lg_u32 s15, 0
	s_cselect_b64 s[0:1], -1, 0
	s_cmp_eq_u32 s15, 0
	s_cbranch_scc1 .LBB0_702
	s_waitcnt lgkmcnt(8)
	v_mfma_f32_16x16x32_bf16 v[130:133], v[98:101], v[66:69], 0
	v_mfma_f32_16x16x32_bf16 v[134:137], v[102:105], v[66:69], 0
	v_mfma_f32_16x16x32_bf16 v[130:133], v[106:109], v[70:73], v[130:133]
	v_mfma_f32_16x16x32_bf16 v[134:137], v[110:113], v[70:73], v[134:137]
	v_mfma_f32_16x16x32_bf16 v[130:133], v[114:117], v[74:77], v[130:133]
	v_mfma_f32_16x16x32_bf16 v[134:137], v[118:121], v[74:77], v[134:137]
	v_mfma_f32_16x16x32_bf16 v[162:165], v[122:125], v[78:81], v[130:133]
	v_mfma_f32_16x16x32_bf16 v[166:169], v[126:129], v[78:81], v[134:137]
	s_waitcnt lgkmcnt(0)
	v_mfma_f32_16x16x32_bf16 v[130:133], v[146:149], v[66:69], 0
	v_mfma_f32_16x16x32_bf16 v[134:137], v[150:153], v[66:69], 0
	v_mfma_f32_16x16x32_bf16 v[130:133], v[170:173], v[70:73], v[130:133]
	v_mfma_f32_16x16x32_bf16 v[134:137], v[174:177], v[70:73], v[134:137]
	v_mfma_f32_16x16x32_bf16 v[130:133], v[178:181], v[74:77], v[130:133]
	v_mfma_f32_16x16x32_bf16 v[134:137], v[182:185], v[74:77], v[134:137]
	v_mfma_f32_16x16x32_bf16 v[154:157], v[186:189], v[78:81], v[130:133]
	v_mfma_f32_16x16x32_bf16 v[158:161], v[190:193], v[78:81], v[134:137]
.LBB0_702:
	s_and_b32 s15, s78, 0xf0
	s_cmp_lg_u32 s15, 0
	s_cselect_b64 s[20:21], -1, 0
	s_cmp_eq_u32 s15, 0
	s_cbranch_scc1 .LBB0_704
	s_waitcnt lgkmcnt(8)
	v_mfma_f32_16x16x32_bf16 v[98:101], v[98:101], v[82:85], 0
	v_mfma_f32_16x16x32_bf16 v[102:105], v[102:105], v[82:85], 0
	v_mfma_f32_16x16x32_bf16 v[98:101], v[106:109], v[86:89], v[98:101]
	v_mfma_f32_16x16x32_bf16 v[102:105], v[110:113], v[86:89], v[102:105]
	v_mfma_f32_16x16x32_bf16 v[98:101], v[114:117], v[90:93], v[98:101]
	v_mfma_f32_16x16x32_bf16 v[102:105], v[118:121], v[90:93], v[102:105]
	v_mfma_f32_16x16x32_bf16 v[138:141], v[122:125], v[94:97], v[98:101]
	v_mfma_f32_16x16x32_bf16 v[142:145], v[126:129], v[94:97], v[102:105]
	s_waitcnt lgkmcnt(0)
	v_mfma_f32_16x16x32_bf16 v[98:101], v[146:149], v[82:85], 0
	v_mfma_f32_16x16x32_bf16 v[102:105], v[150:153], v[82:85], 0
	v_mfma_f32_16x16x32_bf16 v[98:101], v[170:173], v[86:89], v[98:101]
	v_mfma_f32_16x16x32_bf16 v[102:105], v[174:177], v[86:89], v[102:105]
	v_mfma_f32_16x16x32_bf16 v[98:101], v[178:181], v[90:93], v[98:101]
	v_mfma_f32_16x16x32_bf16 v[102:105], v[182:185], v[90:93], v[102:105]
	v_mfma_f32_16x16x32_bf16 v[130:133], v[186:189], v[94:97], v[98:101]
	v_mfma_f32_16x16x32_bf16 v[134:137], v[190:193], v[94:97], v[102:105]

; #define LAS __attribute__((address_space(3)))
; #define TA_SB __builtin_amdgcn_sched_barrier(0)
; __device__ __forceinline__ void ta_ldk(LAS const unsigned char* kb, int kg, int i, int g4, bf16x8 (&a0)[4], bf16x8 (&a1)[4]) {
;     LAS const unsigned char* kr = kb + (32 * kg + 8 * (i >> 2) + (i & 3)) * 256;
; #pragma unroll
;     for (int ks = 0; ks < 4; ++ks) { const int co = ((4 * ks + g4) ^ i) * 16; a0[ks] = *(LAS const bf16x8*)(kr + co); a1[ks] = *(LAS const bf16x8*)(kr + 4 * 256 + co); } }
; __device__ __forceinline__ void ta_ldv(LAS const unsigned char* vb, int kg, int i, int g4, bf16x8 (&vt)[8]) {
;     LAS const unsigned char* vr = vb + i * 128 + (((4 * kg + g4) ^ ((i >> 1) & 7)) * 16);
; #pragma unroll
;     for (int dt = 0; dt < 8; ++dt) vt[dt] = *(LAS const bf16x8*)(vr + dt * 16 * 128); }
; __device__ __forceinline__ void ta_qk(const bf16x8 (&a0)[4], const bf16x8 (&a1)[4], const QF& q, f32x4& s0, f32x4& s1) {
;     s0 = (f32x4){0.f, 0.f, 0.f, 0.f}; s1 = (f32x4){0.f, 0.f, 0.f, 0.f};
; #pragma unroll
;     for (int ks = 0; ks < 4; ++ks) { s0 = __builtin_amdgcn_mfma_f32_16x16x32_bf16(a0[ks], q.f[ks], s0, 0, 0, 0); s1 = __builtin_amdgcn_mfma_f32_16x16x32_bf16(a1[ks], q.f[ks], s1, 0, 0, 0); } }
; template <int MODE, bool FULL = false> __device__ __forceinline__ void ta_compute2(LAS const unsigned char* kb, const QF& q0, const QF& q1, f32x4 (&O0)[8], f32x4 (&O1)[8], float& l0, float& l1, int i, int g4, int tq0, int tq1, bool n0, bool n1, bool cv0, bool cv1, int kbase, float mb, bool full = fa ...
;     LAS const unsigned char* vb = kb + 16384;
;     const float m0 = cv0 ? mb : 1e30f, m1 = cv1 ? mb : 1e30f;
;     bf16x8 ka0[4], ka1[4], kb0[4], kb1[4], va[8], vc[8]; f32x4 s0, s1, t0, t1, u0, u1, v0, v1; bf16x8 pa0, pb0, pa1, pb1;
;     ta_ldk(kb, 0, i, g4, ka0, ka1); ta_ldk(kb, 1, i, g4, kb0, kb1); TA_SB;
;     if (n0) { ta_qk(ka0, ka1, q0, s0, s1); ta_qk(kb0, kb1, q0, t0, t1); } TA_SB;
;     if (n1) { ta_qk(ka0, ka1, q1, u0, u1); ta_qk(kb0, kb1, q1, v0, v1); } TA_SB;
.LBB0_722:
.LBB0_723:
	s_cmp_ge_i32 s77, s74
	s_cbranch_scc1 .LBB0_748
	s_waitcnt lgkmcnt(0)
	v_mov_b32_e32 v136, s87
	s_add_i32 s0, s75, 0x8000
	s_and_b32 s0, s0, 0x18000
	s_mov_b32 s77, s89
	s_cmp_eq_u32 s77, 0
	s_cbranch_scc1 .LBB0_748
	s_add_i32 s14, s0, 0
	v_add_u32_e32 v122, s14, v233
	v_add_u32_e32 v130, v122, v234
	v_add_u32_e32 v131, v122, v235
	v_add_u32_e32 v137, v122, v236
	v_add_u32_e32 v138, v122, v237
	ds_read_b128 v[98:101], v130
	ds_read_b128 v[102:105], v130 offset:1024
	ds_read_b128 v[106:109], v131
	ds_read_b128 v[110:113], v131 offset:1024
	ds_read_b128 v[114:117], v137
	ds_read_b128 v[118:121], v137 offset:1024
	ds_read_b128 v[122:125], v138
	ds_read_b128 v[126:129], v138 offset:1024
	ds_read_b128 v[132:135], v130 offset:8192
	ds_read_b128 v[150:153], v130 offset:9216
	ds_read_b128 v[170:173], v131 offset:8192
	ds_read_b128 v[174:177], v131 offset:9216
	ds_read_b128 v[178:181], v137 offset:8192
	ds_read_b128 v[182:185], v137 offset:9216
	ds_read_b128 v[186:189], v138 offset:8192
	ds_read_b128 v[190:193], v138 offset:9216
	s_and_b32 s15, s77, 15
	s_cmp_lg_u32 s15, 0
	s_cselect_b64 s[0:1], -1, 0
	s_cmp_eq_u32 s15, 0
	s_cbranch_scc1 .LBB0_727
	s_waitcnt lgkmcnt(8)
	v_mfma_f32_16x16x32_bf16 v[138:141], v[98:101], v[66:69], 0
	v_mfma_f32_16x16x32_bf16 v[142:145], v[102:105], v[66:69], 0
	v_mfma_f32_16x16x32_bf16 v[138:141], v[106:109], v[70:73], v[138:141]
	v_mfma_f32_16x16x32_bf16 v[142:145], v[110:113], v[70:73], v[142:145]
	v_mfma_f32_16x16x32_bf16 v[138:141], v[114:117], v[74:77], v[138:141]
	v_mfma_f32_16x16x32_bf16 v[142:145], v[118:121], v[74:77], v[142:145]
	v_mfma_f32_16x16x32_bf16 v[162:165], v[122:125], v[78:81], v[138:141]
	v_mfma_f32_16x16x32_bf16 v[166:169], v[126:129], v[78:81], v[142:145]
	s_waitcnt lgkmcnt(0)
	v_mfma_f32_16x16x32_bf16 v[138:141], v[132:135], v[66:69], 0
	v_mfma_f32_16x16x32_bf16 v[142:145], v[150:153], v[66:69], 0
	v_mfma_f32_16x16x32_bf16 v[138:141], v[170:173], v[70:73], v[138:141]
	v_mfma_f32_16x16x32_bf16 v[142:145], v[174:177], v[70:73], v[142:145]
	v_mfma_f32_16x16x32_bf16 v[138:141], v[178:181], v[74:77], v[138:141]
	v_mfma_f32_16x16x32_bf16 v[142:145], v[182:185], v[74:77], v[142:145]
	v_mfma_f32_16x16x32_bf16 v[154:157], v[186:189], v[78:81], v[138:141]
	v_mfma_f32_16x16x32_bf16 v[158:161], v[190:193], v[78:81], v[142:145]
.LBB0_727:
	s_and_b32 s15, s77, 0xf0
	s_cmp_lg_u32 s15, 0
	s_cselect_b64 s[20:21], -1, 0
	s_cmp_eq_u32 s15, 0
	s_cbranch_scc1 .LBB0_729
	s_waitcnt lgkmcnt(8)
	v_mfma_f32_16x16x32_bf16 v[98:101], v[98:101], v[82:85], 0
	v_mfma_f32_16x16x32_bf16 v[102:105], v[102:105], v[82:85], 0
	v_mfma_f32_16x16x32_bf16 v[98:101], v[106:109], v[86:89], v[98:101]
	v_mfma_f32_16x16x32_bf16 v[102:105], v[110:113], v[86:89], v[102:105]
	v_mfma_f32_16x16x32_bf16 v[98:101], v[114:117], v[90:93], v[98:101]
	v_mfma_f32_16x16x32_bf16 v[102:105], v[118:121], v[90:93], v[102:105]
	v_mfma_f32_16x16x32_bf16 v[142:145], v[122:125], v[94:97], v[98:101]
	v_mfma_f32_16x16x32_bf16 v[146:149], v[126:129], v[94:97], v[102:105]
	s_waitcnt lgkmcnt(0)
	v_mfma_f32_16x16x32_bf16 v[98:101], v[132:135], v[82:85], 0
	v_mfma_f32_16x16x32_bf16 v[102:105], v[150:153], v[82:85], 0
	v_mfma_f32_16x16x32_bf16 v[98:101], v[170:173], v[86:89], v[98:101]
	v_mfma_f32_16x16x32_bf16 v[102:105], v[174:177], v[86:89], v[102:105]
	v_mfma_f32_16x16x32_bf16 v[98:101], v[178:181], v[90:93], v[98:101]
	v_mfma_f32_16x16x32_bf16 v[102:105], v[182:185], v[90:93], v[102:105]
	v_mfma_f32_16x16x32_bf16 v[130:133], v[186:189], v[94:97], v[98:101]
	v_mfma_f32_16x16x32_bf16 v[138:141], v[190:193], v[94:97], v[102:105]
